# K1: first 16 loads issued at top of prologue; epilogue wave sums via DPP row_bcast instead of ds_bpermute
# speedup vs baseline: 1.0969x; 1.0114x over previous
.LBB0_6:
	s_lshr_b32 s12, s2, 3
	s_mov_b32 s13, 0
	s_and_b32 s3, s2, 7
	s_lshl_b64 s[0:1], s[12:13], 20
	v_lshrrev_b32_e32 v62, 6, v0
	v_and_b32_e32 v1, 63, v0
	v_lshlrev_b32_e32 v2, 13, v62
	v_lshlrev_b32_e32 v63, 4, v1
	v_lshl_add_u32 v2, s3, 17, v2
	v_or_b32_e32 v68, v2, v63
	s_mov_b32 s11, 0x20000
	s_mov_b32 s10, 0x100000
	s_waitcnt lgkmcnt(0)
	s_add_u32 s8, s4, s0
	s_addc_u32 s9, s5, s1
	s_and_b32 s9, s9, 0xffff
	v_mov_b32_e32 v46, v68
	buffer_load_dwordx4 v[26:29], v46, s[8:11], 0 offen sc0 nt
	buffer_load_dwordx4 v[34:37], v46, s[8:11], 0 offen offset:2048 sc0 nt
	buffer_load_dwordx4 v[10:13], v46, s[8:11], 0 offen offset:1024 sc0 nt
	buffer_load_dwordx4 v[14:17], v46, s[8:11], 0 offen offset:3072 sc0 nt
	v_add_u32_e32 v47, 0x1000, v46
	buffer_load_dwordx4 v[30:33], v47, s[8:11], 0 offen sc0 nt
	buffer_load_dwordx4 v[38:41], v47, s[8:11], 0 offen offset:2048 sc0 nt
	buffer_load_dwordx4 v[18:21], v47, s[8:11], 0 offen offset:1024 sc0 nt
	buffer_load_dwordx4 v[22:25], v47, s[8:11], 0 offen offset:3072 sc0 nt
	v_add_u32_e32 v46, 0x8000, v68
	buffer_load_dwordx4 v[96:99], v46, s[8:11], 0 offen sc0 nt
	buffer_load_dwordx4 v[104:107], v46, s[8:11], 0 offen offset:2048 sc0 nt
	buffer_load_dwordx4 v[80:83], v46, s[8:11], 0 offen offset:1024 sc0 nt
	buffer_load_dwordx4 v[84:87], v46, s[8:11], 0 offen offset:3072 sc0 nt
	v_add_u32_e32 v47, 0x1000, v46
	buffer_load_dwordx4 v[100:103], v47, s[8:11], 0 offen sc0 nt
	buffer_load_dwordx4 v[108:111], v47, s[8:11], 0 offen offset:2048 sc0 nt
	buffer_load_dwordx4 v[88:91], v47, s[8:11], 0 offen offset:1024 sc0 nt
	buffer_load_dwordx4 v[92:95], v47, s[8:11], 0 offen offset:3072 sc0 nt
	v_mbcnt_lo_u32_b32 v3, -1, 0
	v_mbcnt_hi_u32_b32 v3, -1, v3
	s_lshr_b32 s12, s2, 3
	s_mov_b32 s13, 0
	v_and_b32_e32 v5, 64, v3
	s_and_b32 s3, s2, 7
	s_lshl_b64 s[0:1], s[12:13], 20
	v_xor_b32_e32 v4, 16, v3
	v_add_u32_e32 v5, 64, v5
	s_waitcnt lgkmcnt(0)
	s_add_u32 s8, s4, s0
	v_cmp_lt_i32_e32 vcc, v4, v5
	v_lshrrev_b32_e32 v62, 6, v0
	s_addc_u32 s0, s5, s1
	s_lshl_b32 s12, s12, 9
	v_cndmask_b32_e32 v4, v3, v4, vcc
	s_and_b32 s9, s0, 0xffff
	v_lshlrev_b32_e32 v2, 2, v62
	v_lshlrev_b32_e32 v65, 2, v4
	v_xor_b32_e32 v4, 32, v3
	s_lshl_b64 s[4:5], s[12:13], 2
	v_and_b32_e32 v1, 63, v0
	v_cmp_lt_i32_e32 vcc, v4, v5
	v_lshl_add_u32 v66, s3, 6, v2
	s_add_u32 s4, s6, s4
	v_lshlrev_b32_e32 v2, 13, v62
	v_lshlrev_b32_e32 v63, 4, v1
	v_cndmask_b32_e32 v3, v3, v4, vcc
	v_lshlrev_b32_e32 v42, 2, v66
	v_mov_b32_e32 v43, 0
	s_addc_u32 s5, s7, s5
	v_lshl_add_u32 v2, s3, 17, v2
	s_mov_b32 s11, 0x20000
	s_mov_b32 s10, 0x100000
	v_lshlrev_b32_e32 v64, 2, v3
	v_cmp_eq_u32_e64 s[0:1], 0, v1
	v_lshl_add_u64 v[44:45], s[4:5], 0, v[42:43]
	v_lshrrev_b32_e32 v67, 2, v66
	v_or_b32_e32 v68, v2, v63
	v_mov_b32_e32 v42, v43
	v_mov_b32_e32 v2, v43
	v_mov_b32_e32 v3, v43
	v_mov_b32_e32 v4, v43
	v_mov_b32_e32 v5, v43
	v_mov_b32_e32 v6, v43
	v_mov_b32_e32 v7, v43
	v_mov_b32_e32 v8, v43
	v_mov_b32_e32 v9, v43
	s_sub_u32 s14, s2, 64
	s_cmp_lt_u32 s14, 6
	s_cbranch_scc0 .Lk1_nozero
	v_lshlrev_b32_e32 v69, 4, v0
	s_lshl_b32 s14, s14, 12
	v_add_u32_e32 v69, s14, v69
	v_add_u32_e32 v69, 0x582000, v69
	global_store_dwordx4 v69, v[2:5], s[6:7]

.LBB0_8:
	s_bitcmp1_b32 s15, 8
	s_cselect_b64 s[20:21], -1, 0
	s_lshr_b32 s16, s15, 2
	s_and_b32 s16, s16, 63
	s_lshl_b64 s[4:5], 1, s16
	s_waitcnt vmcnt(12)
	v_pk_add_f32 v[72:73], v[26:27], v[28:29]
	v_pk_add_f32 v[74:75], v[10:11], v[12:13]
	v_pk_add_f32 v[76:77], v[34:35], v[36:37]
	v_pk_add_f32 v[78:79], v[14:15], v[16:17]
	v_pk_add_f32 v[58:59], v[26:27], v[34:35]
	v_pk_add_f32 v[60:61], v[28:29], v[36:37]
	v_pk_add_f32 v[72:73], v[72:73], v[74:75]
	v_pk_add_f32 v[76:77], v[76:77], v[78:79]
	v_pk_add_f32 v[54:55], v[10:11], v[14:15]
	v_pk_add_f32 v[56:57], v[12:13], v[16:17]
	v_add_f32_e32 v50, v72, v73
	v_add_f32_e32 v51, v76, v77
	s_waitcnt vmcnt(8)
	v_pk_add_f32 v[72:73], v[30:31], v[32:33]
	v_pk_add_f32 v[74:75], v[18:19], v[20:21]
	v_pk_add_f32 v[76:77], v[38:39], v[40:41]
	v_pk_add_f32 v[78:79], v[22:23], v[24:25]
	v_pk_add_f32 v[48:49], v[30:31], v[38:39]
	v_pk_add_f32 v[70:71], v[32:33], v[40:41]
	v_pk_add_f32 v[72:73], v[72:73], v[74:75]
	v_pk_add_f32 v[76:77], v[76:77], v[78:79]
	v_pk_add_f32 v[58:59], v[58:59], v[48:49]
	v_pk_add_f32 v[60:61], v[60:61], v[70:71]
	v_pk_add_f32 v[48:49], v[18:19], v[22:23]
	v_pk_add_f32 v[70:71], v[20:21], v[24:25]
	v_add_f32_e32 v52, v72, v73
	v_add_f32_e32 v53, v76, v77
	v_pk_add_f32 v[2:3], v[2:3], v[58:59]
	v_pk_add_f32 v[4:5], v[4:5], v[60:61]
	v_pk_add_f32 v[54:55], v[54:55], v[48:49]
	v_pk_add_f32 v[56:57], v[56:57], v[70:71]
	v_add_f32_e32 v72, v50, v51
	v_add_f32_e32 v73, v52, v53
	v_pk_add_f32 v[6:7], v[6:7], v[54:55]
	v_pk_add_f32 v[8:9], v[8:9], v[56:57]
	v_add_f32_e32 v72, v72, v73
	v_add_f32_e32 v43, v43, v72
	v_add_f32_dpp v50, v50, v50 quad_perm:[1,0,3,2] row_mask:0xf bank_mask:0xf
	v_add_f32_dpp v51, v51, v51 quad_perm:[1,0,3,2] row_mask:0xf bank_mask:0xf
	v_add_f32_dpp v52, v52, v52 quad_perm:[1,0,3,2] row_mask:0xf bank_mask:0xf
	v_add_f32_dpp v53, v53, v53 quad_perm:[1,0,3,2] row_mask:0xf bank_mask:0xf
	v_add_f32_dpp v50, v50, v50 quad_perm:[2,3,0,1] row_mask:0xf bank_mask:0xf
	v_add_f32_dpp v51, v51, v51 quad_perm:[2,3,0,1] row_mask:0xf bank_mask:0xf
	v_add_f32_dpp v52, v52, v52 quad_perm:[2,3,0,1] row_mask:0xf bank_mask:0xf
	v_add_f32_dpp v53, v53, v53 quad_perm:[2,3,0,1] row_mask:0xf bank_mask:0xf
	v_add_f32_dpp v50, v50, v50 row_half_mirror row_mask:0xf bank_mask:0xf
	v_add_f32_dpp v51, v51, v51 row_half_mirror row_mask:0xf bank_mask:0xf
	v_add_f32_dpp v52, v52, v52 row_half_mirror row_mask:0xf bank_mask:0xf
	v_add_f32_dpp v53, v53, v53 row_half_mirror row_mask:0xf bank_mask:0xf
	v_add_f32_dpp v50, v50, v50 row_mirror row_mask:0xf bank_mask:0xf
	v_add_f32_dpp v51, v51, v51 row_mirror row_mask:0xf bank_mask:0xf
	v_add_f32_dpp v52, v52, v52 row_mirror row_mask:0xf bank_mask:0xf
	v_add_f32_dpp v53, v53, v53 row_mirror row_mask:0xf bank_mask:0xf
	v_add_f32_dpp v50, v50, v50 row_bcast:15 row_mask:0xa bank_mask:0xf
	v_add_f32_dpp v51, v51, v51 row_bcast:15 row_mask:0xa bank_mask:0xf
	v_add_f32_dpp v52, v52, v52 row_bcast:15 row_mask:0xa bank_mask:0xf
	v_add_f32_dpp v53, v53, v53 row_bcast:15 row_mask:0xa bank_mask:0xf
	v_add_f32_dpp v50, v50, v50 row_bcast:31 row_mask:0xc bank_mask:0xf
	v_add_f32_dpp v51, v51, v51 row_bcast:31 row_mask:0xc bank_mask:0xf
	v_add_f32_dpp v52, v52, v52 row_bcast:31 row_mask:0xc bank_mask:0xf
	v_add_f32_dpp v53, v53, v53 row_bcast:31 row_mask:0xc bank_mask:0xf
	s_mov_b64 exec, s[4:5]
	v_cndmask_b32_e64 v58, v26, v10, s[20:21]
	v_cndmask_b32_e64 v59, v35, v15, s[20:21]
	v_cndmask_b32_e64 v60, v32, v20, s[20:21]
	v_cndmask_b32_e64 v61, v41, v25, s[20:21]
	global_store_dwordx4 v[44:45], v[58:61], off
	v_add_f32_e32 v72, v58, v59
	v_add_f32_e32 v73, v60, v61
	v_add_f32_e32 v72, v72, v73
	v_add_f32_e32 v42, v42, v72
	s_mov_b32 s4, 0
	s_brev_b32 s5, 1
	s_mov_b64 exec, s[4:5]
	v_lshl_add_u64 v[72:73], v[44:45], 0, s[18:19]
	global_store_dwordx4 v[72:73], v[50:53], off
	s_mov_b64 exec, -1
	s_add_u32 s15, s15, 16
	v_lshl_add_u64 v[44:45], v[44:45], 0, 64
	v_add_u32_e32 v46, 0x10000, v68
	buffer_load_dwordx4 v[26:29], v46, s[8:11], 0 offen sc0 nt
	buffer_load_dwordx4 v[34:37], v46, s[8:11], 0 offen offset:2048 sc0 nt
	buffer_load_dwordx4 v[10:13], v46, s[8:11], 0 offen offset:1024 sc0 nt
	buffer_load_dwordx4 v[14:17], v46, s[8:11], 0 offen offset:3072 sc0 nt
	v_add_u32_e32 v47, 0x1000, v46
	buffer_load_dwordx4 v[30:33], v47, s[8:11], 0 offen sc0 nt
	buffer_load_dwordx4 v[38:41], v47, s[8:11], 0 offen offset:2048 sc0 nt
	buffer_load_dwordx4 v[18:21], v47, s[8:11], 0 offen offset:1024 sc0 nt
	buffer_load_dwordx4 v[22:25], v47, s[8:11], 0 offen offset:3072 sc0 nt
	s_bitcmp1_b32 s15, 8
	s_cselect_b64 s[20:21], -1, 0
	s_lshr_b32 s16, s15, 2
	s_and_b32 s16, s16, 63
	s_lshl_b64 s[4:5], 1, s16
	s_waitcnt vmcnt(14)
	v_pk_add_f32 v[72:73], v[96:97], v[98:99]
	v_pk_add_f32 v[74:75], v[80:81], v[82:83]
	v_pk_add_f32 v[76:77], v[104:105], v[106:107]
	v_pk_add_f32 v[78:79], v[84:85], v[86:87]
	v_pk_add_f32 v[58:59], v[96:97], v[104:105]
	v_pk_add_f32 v[60:61], v[98:99], v[106:107]
	v_pk_add_f32 v[72:73], v[72:73], v[74:75]
	v_pk_add_f32 v[76:77], v[76:77], v[78:79]
	v_pk_add_f32 v[54:55], v[80:81], v[84:85]
	v_pk_add_f32 v[56:57], v[82:83], v[86:87]
	v_add_f32_e32 v50, v72, v73
	v_add_f32_e32 v51, v76, v77
	s_waitcnt vmcnt(10)
	v_pk_add_f32 v[72:73], v[100:101], v[102:103]
	v_pk_add_f32 v[74:75], v[88:89], v[90:91]
	v_pk_add_f32 v[76:77], v[108:109], v[110:111]
	v_pk_add_f32 v[78:79], v[92:93], v[94:95]
	v_pk_add_f32 v[48:49], v[100:101], v[108:109]
	v_pk_add_f32 v[70:71], v[102:103], v[110:111]
	v_pk_add_f32 v[72:73], v[72:73], v[74:75]
	v_pk_add_f32 v[76:77], v[76:77], v[78:79]
	v_pk_add_f32 v[58:59], v[58:59], v[48:49]
	v_pk_add_f32 v[60:61], v[60:61], v[70:71]
	v_pk_add_f32 v[48:49], v[88:89], v[92:93]
	v_pk_add_f32 v[70:71], v[90:91], v[94:95]
	v_add_f32_e32 v52, v72, v73
	v_add_f32_e32 v53, v76, v77
	v_pk_add_f32 v[2:3], v[2:3], v[58:59]
	v_pk_add_f32 v[4:5], v[4:5], v[60:61]
	v_pk_add_f32 v[54:55], v[54:55], v[48:49]
	v_pk_add_f32 v[56:57], v[56:57], v[70:71]
	v_add_f32_e32 v72, v50, v51
	v_add_f32_e32 v73, v52, v53
	v_pk_add_f32 v[6:7], v[6:7], v[54:55]
	v_pk_add_f32 v[8:9], v[8:9], v[56:57]
	v_add_f32_e32 v72, v72, v73
	v_add_f32_e32 v43, v43, v72
	v_add_f32_dpp v50, v50, v50 quad_perm:[1,0,3,2] row_mask:0xf bank_mask:0xf
	v_add_f32_dpp v51, v51, v51 quad_perm:[1,0,3,2] row_mask:0xf bank_mask:0xf
	v_add_f32_dpp v52, v52, v52 quad_perm:[1,0,3,2] row_mask:0xf bank_mask:0xf
	v_add_f32_dpp v53, v53, v53 quad_perm:[1,0,3,2] row_mask:0xf bank_mask:0xf
	v_add_f32_dpp v50, v50, v50 quad_perm:[2,3,0,1] row_mask:0xf bank_mask:0xf
	v_add_f32_dpp v51, v51, v51 quad_perm:[2,3,0,1] row_mask:0xf bank_mask:0xf
	v_add_f32_dpp v52, v52, v52 quad_perm:[2,3,0,1] row_mask:0xf bank_mask:0xf
	v_add_f32_dpp v53, v53, v53 quad_perm:[2,3,0,1] row_mask:0xf bank_mask:0xf
	v_add_f32_dpp v50, v50, v50 row_half_mirror row_mask:0xf bank_mask:0xf
	v_add_f32_dpp v51, v51, v51 row_half_mirror row_mask:0xf bank_mask:0xf
	v_add_f32_dpp v52, v52, v52 row_half_mirror row_mask:0xf bank_mask:0xf
	v_add_f32_dpp v53, v53, v53 row_half_mirror row_mask:0xf bank_mask:0xf
	v_add_f32_dpp v50, v50, v50 row_mirror row_mask:0xf bank_mask:0xf
	v_add_f32_dpp v51, v51, v51 row_mirror row_mask:0xf bank_mask:0xf
	v_add_f32_dpp v52, v52, v52 row_mirror row_mask:0xf bank_mask:0xf
	v_add_f32_dpp v53, v53, v53 row_mirror row_mask:0xf bank_mask:0xf
	v_add_f32_dpp v50, v50, v50 row_bcast:15 row_mask:0xa bank_mask:0xf
	v_add_f32_dpp v51, v51, v51 row_bcast:15 row_mask:0xa bank_mask:0xf
	v_add_f32_dpp v52, v52, v52 row_bcast:15 row_mask:0xa bank_mask:0xf
	v_add_f32_dpp v53, v53, v53 row_bcast:15 row_mask:0xa bank_mask:0xf
	v_add_f32_dpp v50, v50, v50 row_bcast:31 row_mask:0xc bank_mask:0xf
	v_add_f32_dpp v51, v51, v51 row_bcast:31 row_mask:0xc bank_mask:0xf
	v_add_f32_dpp v52, v52, v52 row_bcast:31 row_mask:0xc bank_mask:0xf
	v_add_f32_dpp v53, v53, v53 row_bcast:31 row_mask:0xc bank_mask:0xf
	s_mov_b64 exec, s[4:5]
	v_cndmask_b32_e64 v58, v96, v80, s[20:21]
	v_cndmask_b32_e64 v59, v105, v85, s[20:21]
	v_cndmask_b32_e64 v60, v102, v90, s[20:21]
	v_cndmask_b32_e64 v61, v111, v95, s[20:21]
	global_store_dwordx4 v[44:45], v[58:61], off
	v_add_f32_e32 v72, v58, v59
	v_add_f32_e32 v73, v60, v61
	v_add_f32_e32 v72, v72, v73
	v_add_f32_e32 v42, v42, v72
	s_mov_b32 s4, 0
	s_brev_b32 s5, 1
	s_mov_b64 exec, s[4:5]
	v_lshl_add_u64 v[72:73], v[44:45], 0, s[18:19]
	global_store_dwordx4 v[72:73], v[50:53], off
	s_mov_b64 exec, -1
	s_add_u32 s15, s15, 16
	v_lshl_add_u64 v[44:45], v[44:45], 0, 64
	v_add_u32_e32 v46, 0x18000, v68
	buffer_load_dwordx4 v[96:99], v46, s[8:11], 0 offen sc0 nt
	buffer_load_dwordx4 v[104:107], v46, s[8:11], 0 offen offset:2048 sc0 nt
	buffer_load_dwordx4 v[80:83], v46, s[8:11], 0 offen offset:1024 sc0 nt
	buffer_load_dwordx4 v[84:87], v46, s[8:11], 0 offen offset:3072 sc0 nt
	v_add_u32_e32 v47, 0x1000, v46
	buffer_load_dwordx4 v[100:103], v47, s[8:11], 0 offen sc0 nt
	buffer_load_dwordx4 v[108:111], v47, s[8:11], 0 offen offset:2048 sc0 nt
	buffer_load_dwordx4 v[88:91], v47, s[8:11], 0 offen offset:1024 sc0 nt
	buffer_load_dwordx4 v[92:95], v47, s[8:11], 0 offen offset:3072 sc0 nt
	s_bitcmp1_b32 s15, 8
	s_cselect_b64 s[20:21], -1, 0
	s_lshr_b32 s16, s15, 2
	s_and_b32 s16, s16, 63
	s_lshl_b64 s[4:5], 1, s16
	s_waitcnt vmcnt(14)
	v_pk_add_f32 v[72:73], v[26:27], v[28:29]
	v_pk_add_f32 v[74:75], v[10:11], v[12:13]
	v_pk_add_f32 v[76:77], v[34:35], v[36:37]
	v_pk_add_f32 v[78:79], v[14:15], v[16:17]
	v_pk_add_f32 v[58:59], v[26:27], v[34:35]
	v_pk_add_f32 v[60:61], v[28:29], v[36:37]
	v_pk_add_f32 v[72:73], v[72:73], v[74:75]
	v_pk_add_f32 v[76:77], v[76:77], v[78:79]
	v_pk_add_f32 v[54:55], v[10:11], v[14:15]
	v_pk_add_f32 v[56:57], v[12:13], v[16:17]
	v_add_f32_e32 v50, v72, v73
	v_add_f32_e32 v51, v76, v77
	s_waitcnt vmcnt(10)
	v_pk_add_f32 v[72:73], v[30:31], v[32:33]
	v_pk_add_f32 v[74:75], v[18:19], v[20:21]
	v_pk_add_f32 v[76:77], v[38:39], v[40:41]
	v_pk_add_f32 v[78:79], v[22:23], v[24:25]
	v_pk_add_f32 v[48:49], v[30:31], v[38:39]
	v_pk_add_f32 v[70:71], v[32:33], v[40:41]
	v_pk_add_f32 v[72:73], v[72:73], v[74:75]
	v_pk_add_f32 v[76:77], v[76:77], v[78:79]
	v_pk_add_f32 v[58:59], v[58:59], v[48:49]
	v_pk_add_f32 v[60:61], v[60:61], v[70:71]
	v_pk_add_f32 v[48:49], v[18:19], v[22:23]
	v_pk_add_f32 v[70:71], v[20:21], v[24:25]
	v_add_f32_e32 v52, v72, v73
	v_add_f32_e32 v53, v76, v77
	v_pk_add_f32 v[2:3], v[2:3], v[58:59]
	v_pk_add_f32 v[4:5], v[4:5], v[60:61]
	v_pk_add_f32 v[54:55], v[54:55], v[48:49]
	v_pk_add_f32 v[56:57], v[56:57], v[70:71]
	v_add_f32_e32 v72, v50, v51
	v_add_f32_e32 v73, v52, v53
	v_pk_add_f32 v[6:7], v[6:7], v[54:55]
	v_pk_add_f32 v[8:9], v[8:9], v[56:57]
	v_add_f32_e32 v72, v72, v73
	v_add_f32_e32 v43, v43, v72
	v_add_f32_dpp v50, v50, v50 quad_perm:[1,0,3,2] row_mask:0xf bank_mask:0xf
	v_add_f32_dpp v51, v51, v51 quad_perm:[1,0,3,2] row_mask:0xf bank_mask:0xf
	v_add_f32_dpp v52, v52, v52 quad_perm:[1,0,3,2] row_mask:0xf bank_mask:0xf
	v_add_f32_dpp v53, v53, v53 quad_perm:[1,0,3,2] row_mask:0xf bank_mask:0xf
	v_add_f32_dpp v50, v50, v50 quad_perm:[2,3,0,1] row_mask:0xf bank_mask:0xf
	v_add_f32_dpp v51, v51, v51 quad_perm:[2,3,0,1] row_mask:0xf bank_mask:0xf
	v_add_f32_dpp v52, v52, v52 quad_perm:[2,3,0,1] row_mask:0xf bank_mask:0xf
	v_add_f32_dpp v53, v53, v53 quad_perm:[2,3,0,1] row_mask:0xf bank_mask:0xf
	v_add_f32_dpp v50, v50, v50 row_half_mirror row_mask:0xf bank_mask:0xf
	v_add_f32_dpp v51, v51, v51 row_half_mirror row_mask:0xf bank_mask:0xf
	v_add_f32_dpp v52, v52, v52 row_half_mirror row_mask:0xf bank_mask:0xf
	v_add_f32_dpp v53, v53, v53 row_half_mirror row_mask:0xf bank_mask:0xf
	v_add_f32_dpp v50, v50, v50 row_mirror row_mask:0xf bank_mask:0xf
	v_add_f32_dpp v51, v51, v51 row_mirror row_mask:0xf bank_mask:0xf
	v_add_f32_dpp v52, v52, v52 row_mirror row_mask:0xf bank_mask:0xf
	v_add_f32_dpp v53, v53, v53 row_mirror row_mask:0xf bank_mask:0xf
	v_add_f32_dpp v50, v50, v50 row_bcast:15 row_mask:0xa bank_mask:0xf
	v_add_f32_dpp v51, v51, v51 row_bcast:15 row_mask:0xa bank_mask:0xf
	v_add_f32_dpp v52, v52, v52 row_bcast:15 row_mask:0xa bank_mask:0xf
	v_add_f32_dpp v53, v53, v53 row_bcast:15 row_mask:0xa bank_mask:0xf
	v_add_f32_dpp v50, v50, v50 row_bcast:31 row_mask:0xc bank_mask:0xf
	v_add_f32_dpp v51, v51, v51 row_bcast:31 row_mask:0xc bank_mask:0xf
	v_add_f32_dpp v52, v52, v52 row_bcast:31 row_mask:0xc bank_mask:0xf
	v_add_f32_dpp v53, v53, v53 row_bcast:31 row_mask:0xc bank_mask:0xf
	s_mov_b64 exec, s[4:5]
	v_cndmask_b32_e64 v58, v26, v10, s[20:21]
	v_cndmask_b32_e64 v59, v35, v15, s[20:21]
	v_cndmask_b32_e64 v60, v32, v20, s[20:21]
	v_cndmask_b32_e64 v61, v41, v25, s[20:21]
	global_store_dwordx4 v[44:45], v[58:61], off
	v_add_f32_e32 v72, v58, v59
	v_add_f32_e32 v73, v60, v61
	v_add_f32_e32 v72, v72, v73
	v_add_f32_e32 v42, v42, v72
	s_mov_b32 s4, 0
	s_brev_b32 s5, 1
	s_mov_b64 exec, s[4:5]
	v_lshl_add_u64 v[72:73], v[44:45], 0, s[18:19]
	global_store_dwordx4 v[72:73], v[50:53], off
	s_mov_b64 exec, -1
	s_add_u32 s15, s15, 16
	v_lshl_add_u64 v[44:45], v[44:45], 0, 64
	s_bitcmp1_b32 s15, 8
	s_cselect_b64 s[20:21], -1, 0
	s_lshr_b32 s16, s15, 2
	s_and_b32 s16, s16, 63
	s_lshl_b64 s[4:5], 1, s16
	s_waitcnt vmcnt(6)
	v_pk_add_f32 v[72:73], v[96:97], v[98:99]
	v_pk_add_f32 v[74:75], v[80:81], v[82:83]
	v_pk_add_f32 v[76:77], v[104:105], v[106:107]
	v_pk_add_f32 v[78:79], v[84:85], v[86:87]
	v_pk_add_f32 v[58:59], v[96:97], v[104:105]
	v_pk_add_f32 v[60:61], v[98:99], v[106:107]
	v_pk_add_f32 v[72:73], v[72:73], v[74:75]
	v_pk_add_f32 v[76:77], v[76:77], v[78:79]
	v_pk_add_f32 v[54:55], v[80:81], v[84:85]
	v_pk_add_f32 v[56:57], v[82:83], v[86:87]
	v_add_f32_e32 v50, v72, v73
	v_add_f32_e32 v51, v76, v77
	s_waitcnt vmcnt(2)
	v_pk_add_f32 v[72:73], v[100:101], v[102:103]
	v_pk_add_f32 v[74:75], v[88:89], v[90:91]
	v_pk_add_f32 v[76:77], v[108:109], v[110:111]
	v_pk_add_f32 v[78:79], v[92:93], v[94:95]
	v_pk_add_f32 v[48:49], v[100:101], v[108:109]
	v_pk_add_f32 v[70:71], v[102:103], v[110:111]
	v_pk_add_f32 v[72:73], v[72:73], v[74:75]
	v_pk_add_f32 v[76:77], v[76:77], v[78:79]
	v_pk_add_f32 v[58:59], v[58:59], v[48:49]
	v_pk_add_f32 v[60:61], v[60:61], v[70:71]
	v_pk_add_f32 v[48:49], v[88:89], v[92:93]
	v_pk_add_f32 v[70:71], v[90:91], v[94:95]
	v_add_f32_e32 v52, v72, v73
	v_add_f32_e32 v53, v76, v77
	v_pk_add_f32 v[2:3], v[2:3], v[58:59]
	v_pk_add_f32 v[4:5], v[4:5], v[60:61]
	v_pk_add_f32 v[54:55], v[54:55], v[48:49]
	v_pk_add_f32 v[56:57], v[56:57], v[70:71]
	v_add_f32_e32 v72, v50, v51
	v_add_f32_e32 v73, v52, v53
	v_pk_add_f32 v[6:7], v[6:7], v[54:55]
	v_pk_add_f32 v[8:9], v[8:9], v[56:57]
	v_add_f32_e32 v72, v72, v73
	v_add_f32_e32 v43, v43, v72
	v_add_f32_dpp v50, v50, v50 quad_perm:[1,0,3,2] row_mask:0xf bank_mask:0xf
	v_add_f32_dpp v51, v51, v51 quad_perm:[1,0,3,2] row_mask:0xf bank_mask:0xf
	v_add_f32_dpp v52, v52, v52 quad_perm:[1,0,3,2] row_mask:0xf bank_mask:0xf
	v_add_f32_dpp v53, v53, v53 quad_perm:[1,0,3,2] row_mask:0xf bank_mask:0xf
	v_add_f32_dpp v50, v50, v50 quad_perm:[2,3,0,1] row_mask:0xf bank_mask:0xf
	v_add_f32_dpp v51, v51, v51 quad_perm:[2,3,0,1] row_mask:0xf bank_mask:0xf
	v_add_f32_dpp v52, v52, v52 quad_perm:[2,3,0,1] row_mask:0xf bank_mask:0xf
	v_add_f32_dpp v53, v53, v53 quad_perm:[2,3,0,1] row_mask:0xf bank_mask:0xf
	v_add_f32_dpp v50, v50, v50 row_half_mirror row_mask:0xf bank_mask:0xf
	v_add_f32_dpp v51, v51, v51 row_half_mirror row_mask:0xf bank_mask:0xf
	v_add_f32_dpp v52, v52, v52 row_half_mirror row_mask:0xf bank_mask:0xf
	v_add_f32_dpp v53, v53, v53 row_half_mirror row_mask:0xf bank_mask:0xf
	v_add_f32_dpp v50, v50, v50 row_mirror row_mask:0xf bank_mask:0xf
	v_add_f32_dpp v51, v51, v51 row_mirror row_mask:0xf bank_mask:0xf
	v_add_f32_dpp v52, v52, v52 row_mirror row_mask:0xf bank_mask:0xf
	v_add_f32_dpp v53, v53, v53 row_mirror row_mask:0xf bank_mask:0xf
	v_add_f32_dpp v50, v50, v50 row_bcast:15 row_mask:0xa bank_mask:0xf
	v_add_f32_dpp v51, v51, v51 row_bcast:15 row_mask:0xa bank_mask:0xf
	v_add_f32_dpp v52, v52, v52 row_bcast:15 row_mask:0xa bank_mask:0xf
	v_add_f32_dpp v53, v53, v53 row_bcast:15 row_mask:0xa bank_mask:0xf
	v_add_f32_dpp v50, v50, v50 row_bcast:31 row_mask:0xc bank_mask:0xf
	v_add_f32_dpp v51, v51, v51 row_bcast:31 row_mask:0xc bank_mask:0xf
	v_add_f32_dpp v52, v52, v52 row_bcast:31 row_mask:0xc bank_mask:0xf
	v_add_f32_dpp v53, v53, v53 row_bcast:31 row_mask:0xc bank_mask:0xf
	s_mov_b64 exec, s[4:5]
	v_cndmask_b32_e64 v58, v96, v80, s[20:21]
	v_cndmask_b32_e64 v59, v105, v85, s[20:21]
	v_cndmask_b32_e64 v60, v102, v90, s[20:21]
	v_cndmask_b32_e64 v61, v111, v95, s[20:21]
	global_store_dwordx4 v[44:45], v[58:61], off
	v_add_f32_e32 v72, v58, v59
	v_add_f32_e32 v73, v60, v61
	v_add_f32_e32 v72, v72, v73
	v_add_f32_e32 v42, v42, v72
	s_mov_b32 s4, 0
	s_brev_b32 s5, 1
	s_mov_b64 exec, s[4:5]
	v_lshl_add_u64 v[72:73], v[44:45], 0, s[18:19]
	global_store_dwordx4 v[72:73], v[50:53], off
	s_mov_b64 exec, -1
	s_add_u32 s15, s15, 16
	v_lshl_add_u64 v[44:45], v[44:45], 0, 64
.LBB0_12:
.LBB0_20:
	v_lshl_or_b32 v1, v62, 11, v63
	ds_write_b128 v1, v[2:5]
	ds_write_b128 v1, v[6:9] offset:1024
	v_add_f32_dpp v42, v42, v42 quad_perm:[1,0,3,2] row_mask:0xf bank_mask:0xf
	v_add_f32_dpp v43, v43, v43 quad_perm:[1,0,3,2] row_mask:0xf bank_mask:0xf
	s_nop 0
	v_add_f32_dpp v42, v42, v42 quad_perm:[2,3,0,1] row_mask:0xf bank_mask:0xf
	v_add_f32_dpp v43, v43, v43 quad_perm:[2,3,0,1] row_mask:0xf bank_mask:0xf
	s_nop 0
	v_add_f32_dpp v42, v42, v42 row_half_mirror row_mask:0xf bank_mask:0xf
	v_add_f32_dpp v43, v43, v43 row_half_mirror row_mask:0xf bank_mask:0xf
	s_nop 0
	v_add_f32_dpp v42, v42, v42 row_mirror row_mask:0xf bank_mask:0xf
	v_add_f32_dpp v43, v43, v43 row_mirror row_mask:0xf bank_mask:0xf
	s_nop 0
	v_add_f32_dpp v42, v42, v42 row_bcast:15 row_mask:0xa bank_mask:0xf
	v_add_f32_dpp v43, v43, v43 row_bcast:15 row_mask:0xa bank_mask:0xf
	s_nop 0
	v_add_f32_dpp v42, v42, v42 row_bcast:31 row_mask:0xc bank_mask:0xf
	v_add_f32_dpp v43, v43, v43 row_bcast:31 row_mask:0xc bank_mask:0xf
	s_nop 0
	s_mov_b32 s4, 0
	s_brev_b32 s5, 1
	s_mov_b64 exec, s[4:5]
	v_lshlrev_b32_e32 v1, 3, v62
	ds_write_b64 v1, v[42:43] offset:8192
	s_mov_b64 exec, -1
.LBB0_22:
	s_movk_i32 s0, 0x7f
	v_cmp_lt_u32_e32 vcc, s0, v0
	s_waitcnt lgkmcnt(0)
	s_barrier
	s_and_saveexec_b64 s[0:1], vcc
	s_xor_b64 s[0:1], exec, s[0:1]
	s_cbranch_execnz .LBB0_25
	s_andn2_saveexec_b64 s[0:1], s[0:1]
	s_cbranch_execnz .LBB0_28
